# v96 + nt on read-once loads: attention block-prologue Q rows and the retention V slices
# speedup vs baseline: 1.0067x; 1.0067x over previous
.LBB0_265:
	s_and_b32 s47, s36, 7
	v_cvt_f32_ubyte0_e32 v0, s47
	v_sub_f32_e32 v0, 0xc0a00000, v0
	s_mov_b32 s52, 0xc2fc0000
	v_cmp_gt_f32_e32 vcc, s52, v0
	s_and_b64 s[54:55], vcc, exec
	s_cselect_b32 s37, 0xffffffc0, 0
	v_cndmask_b32_e32 v2, 0, v172, vcc
	v_add_f32_e32 v0, v0, v2
	v_exp_f32_e32 v0, v0
	s_ashr_i32 s58, s36, 3
	v_readlane_b32 s85, v250, 57
	v_mov_b32_e32 v2, v169
	v_ldexp_f32 v0, v0, s37
	v_sub_f32_e32 v0, 1.0, v0
	v_log_f32_e32 v17, v0
	s_waitcnt vmcnt(0)
	s_barrier
	v_mul_f32_e32 v0, 0x43000000, v17
	v_cmp_gt_f32_e32 vcc, s52, v0
	s_and_b64 s[36:37], vcc, exec
	s_cselect_b32 s36, 0xffffffc0, 0
	v_cndmask_b32_e32 v0, 0, v172, vcc
	v_fmac_f32_e32 v0, 0x43000000, v17
	v_exp_f32_e32 v0, v0
	s_mul_i32 s37, s58, 0x1080000
	s_add_u32 s37, s85, s37
	ds_write_b128 v173, v[208:211]
	ds_write_b128 v173, v[208:211] offset:8192
	ds_write_b128 v173, v[208:211] offset:16384
	ds_write_b128 v173, v[208:211] offset:24576
	v_ldexp_f32 v164, v0, s36
	s_mul_hi_i32 s36, s58, 0x1080000
	s_addc_u32 s54, s61, s36
	s_lshl_b32 s36, s47, 9
	s_add_u32 s56, s37, s36
	v_lshlrev_b32_e32 v3, 4, v2
	v_lshlrev_b32_e32 v0, 7, v2
	v_and_b32_e32 v4, 0x1f0, v3
	s_addc_u32 s57, s54, 0
	v_and_or_b32 v0, v0, s39, v4
	v_lshl_add_u64 v[14:15], s[56:57], 0, v[0:1]
	v_add_co_u32_e32 v6, vcc, s33, v14
	v_mul_f32_e32 v20, v170, v17
	s_nop 0
	v_addc_co_u32_e32 v7, vcc, 0, v15, vcc
	v_add_co_u32_e32 v10, vcc, s40, v14
	s_mul_i32 s55, s58, 0x2100000
	s_nop 0
	v_addc_co_u32_e32 v11, vcc, 0, v15, vcc
	v_add_co_u32_e32 v18, vcc, s41, v14
	s_mul_hi_i32 s54, s58, 0x2100000
	s_nop 0
	v_addc_co_u32_e32 v19, vcc, 0, v15, vcc
	global_load_dwordx4 v[80:83], v[18:19], off
	v_add_co_u32_e32 v18, vcc, s42, v14
	v_lshlrev_b32_e32 v21, 10, v2
	s_nop 0
	v_addc_co_u32_e32 v19, vcc, 0, v15, vcc
	global_load_dwordx4 v[84:87], v[18:19], off
	v_add_co_u32_e32 v18, vcc, s43, v14
	v_and_b32_e32 v22, 0x70, v3
	s_nop 0
	v_addc_co_u32_e32 v19, vcc, 0, v15, vcc
	global_load_dwordx4 v[88:91], v[18:19], off
	v_add_co_u32_e32 v18, vcc, s44, v14
	global_load_dwordx4 v[2:5], v0, s[56:57]
	s_nop 0
	v_addc_co_u32_e32 v19, vcc, 0, v15, vcc
	v_add_co_u32_e32 v14, vcc, s45, v14
	global_load_dwordx4 v[6:9], v[6:7], off
	s_nop 0
	v_addc_co_u32_e32 v15, vcc, 0, v15, vcc
	v_cmp_gt_f32_e32 vcc, s52, v20
	v_readlane_b32 s52, v250, 48
	v_readlane_b32 s53, v250, 49
	v_cndmask_b32_e32 v0, 0, v172, vcc
	s_add_u32 s37, s52, s55
	v_fmac_f32_e32 v0, v170, v17
	s_addc_u32 s56, s53, s54
	s_lshl_b32 s60, s47, 10
	v_exp_f32_e32 v0, v0
	s_add_u32 s37, s37, s60
	s_addc_u32 s57, s56, 0
	s_lshl_b32 s56, s38, 7
	s_and_b32 s84, s56, 0x380
	global_load_dwordx4 v[92:95], v[18:19], off
	global_load_dwordx4 v[160:163], v[14:15], off
	v_cndmask_b32_e32 v14, 0, v174, vcc
	s_add_u32 s56, s37, s84
	v_ldexp_f32 v193, v0, v14
	s_addc_u32 s57, s57, 0
	v_and_or_b32 v0, v21, s48, v22
	s_mul_i32 s76, s58, 0x1080
	global_load_dwordx4 v[10:13], v[10:11], off
	v_lshl_add_u64 v[14:15], s[56:57], 0, v[0:1]
	global_load_dwordx4 v[64:67], v0, s[56:57] nt
	s_mul_hi_i32 s77, s58, 0x1080
	s_add_u32 s56, s76, s62
	s_addc_u32 s57, s77, 0
	s_lshr_b64 s[56:57], s[56:57], 2
	v_add_co_u32_e32 v14, vcc, s49, v14
	s_or_b32 s56, s56, s47
	s_nop 0
	v_addc_co_u32_e32 v15, vcc, 0, v15, vcc
	s_lshl_b64 s[56:57], s[56:57], 14
	v_readlane_b32 s58, v250, 46
	v_mov_b32_e32 v0, v168
	global_load_dwordx4 v[68:71], v[14:15], off nt
	v_readlane_b32 s59, v250, 47
	s_add_u32 s56, s58, s56
	s_addc_u32 s57, s59, s57
	v_lshlrev_b32_e32 v0, 4, v0
	v_lshl_add_u64 v[14:15], s[56:57], 0, v[0:1]
	v_add_co_u32_e32 v18, vcc, s63, v14
	global_load_dwordx4 v[144:147], v0, s[56:57]
	global_load_dwordx4 v[152:155], v0, s[56:57] offset:1024
	global_load_dwordx4 v[140:143], v0, s[56:57] offset:2048
	global_load_dwordx4 v[136:139], v0, s[56:57] offset:3072
	v_addc_co_u32_e32 v19, vcc, 0, v15, vcc
	v_add_co_u32_e32 v20, vcc, s80, v14
	s_add_u32 s58, s85, s36
	s_nop 0
	v_addc_co_u32_e32 v21, vcc, 0, v15, vcc
	global_load_dwordx4 v[156:159], v[20:21], off offset:-4096
	global_load_dwordx4 v[148:151], v[18:19], off offset:1024
	global_load_dwordx4 v[132:135], v[18:19], off offset:2048
	global_load_dwordx4 v[128:131], v[18:19], off offset:3072
	global_load_dwordx4 v[124:127], v[20:21], off
	global_load_dwordx4 v[120:123], v[20:21], off offset:1024
	global_load_dwordx4 v[112:115], v[20:21], off offset:2048
	global_load_dwordx4 v[108:111], v[20:21], off offset:3072
	v_add_co_u32_e32 v14, vcc, s78, v14
	s_addc_u32 s59, s61, 0
	s_nop 0
	v_addc_co_u32_e32 v15, vcc, 0, v15, vcc
	global_load_dwordx4 v[116:119], v[14:15], off
	global_load_dwordx4 v[104:107], v[14:15], off offset:1024
	global_load_dwordx4 v[100:103], v[14:15], off offset:2048
	global_load_dwordx4 v[96:99], v[14:15], off offset:3072
	s_add_u32 s36, s52, s60
	s_addc_u32 s37, s53, 0
	s_add_u32 s36, s36, s84
	s_addc_u32 s37, s37, 0
	s_and_b32 s38, s38, 7
	s_or_b32 s55, s55, s60
	s_lshl_b32 s38, s38, 7
	s_or_b32 s38, s55, s38
	v_readlane_b32 s52, v250, 62
	v_mov_b32_e32 v16, 0
	s_add_u32 s38, s52, s38
	v_readlane_b32 s52, v250, 63
	v_mov_b32_e32 v166, v164
	v_mov_b32_e32 v167, v164
	s_addc_u32 s60, s52, s54
	s_mov_b64 s[84:85], 0
	v_mov_b32_e32 v17, v16
	v_mov_b32_e32 v18, v16
	v_mov_b32_e32 v19, v16
	v_mov_b32_e32 v20, v16
	v_mov_b32_e32 v21, v16
	v_mov_b32_e32 v22, v16
	v_mov_b32_e32 v23, v16
	v_mov_b32_e32 v24, v16
	v_mov_b32_e32 v25, v16
	v_mov_b32_e32 v26, v16
	v_mov_b32_e32 v27, v16
	v_mov_b32_e32 v28, v16
	v_mov_b32_e32 v29, v16
	v_mov_b32_e32 v30, v16
	v_mov_b32_e32 v31, v16
	v_mov_b32_e32 v32, v16
	v_mov_b32_e32 v33, v16
	v_mov_b32_e32 v34, v16
	v_mov_b32_e32 v35, v16
	v_mov_b32_e32 v36, v16
	v_mov_b32_e32 v37, v16
	v_mov_b32_e32 v38, v16
	v_mov_b32_e32 v39, v16
	v_mov_b32_e32 v40, v16
	v_mov_b32_e32 v41, v16
	v_mov_b32_e32 v42, v16
	v_mov_b32_e32 v43, v16
	v_mov_b32_e32 v44, v16
	v_mov_b32_e32 v45, v16
	v_mov_b32_e32 v46, v16
	v_mov_b32_e32 v47, v16
	s_branch .LBB0_268

.LBB0_267:
	s_add_u32 s56, s76, 0x80
	s_nop 10
	v_cndmask_b32_e64 v0, v62, v78, s[0:1]
	v_cndmask_b32_e64 v9, v63, v79, s[0:1]
	v_cndmask_b32_e64 v8, v60, v76, s[0:1]
	v_cndmask_b32_e64 v7, v58, v74, s[0:1]
	v_cndmask_b32_e64 v6, v56, v72, s[0:1]
	v_cndmask_b32_e64 v5, v54, v70, s[0:1]
	v_cndmask_b32_e64 v4, v52, v68, s[0:1]
	v_cndmask_b32_e64 v3, v50, v66, s[0:1]
	v_cndmask_b32_e64 v2, v48, v64, s[0:1]
	s_addc_u32 s57, s77, 0
	v_cndmask_b32_e64 v10, v61, v77, s[0:1]
	v_cndmask_b32_e64 v11, v59, v75, s[0:1]
	v_cndmask_b32_e64 v12, v57, v73, s[0:1]
	v_cndmask_b32_e64 v13, v55, v71, s[0:1]
	v_cndmask_b32_e64 v14, v53, v69, s[0:1]
	v_cndmask_b32_e64 v15, v51, v67, s[0:1]
	v_cndmask_b32_e64 v80, v49, v65, s[0:1]
	v_cvt_pk_bf16_f32 v2, v2, v80
	v_cvt_pk_bf16_f32 v3, v3, v15
	v_cvt_pk_bf16_f32 v4, v4, v14
	v_cvt_pk_bf16_f32 v5, v5, v13
	v_cvt_pk_bf16_f32 v6, v6, v12
	v_cvt_pk_bf16_f32 v7, v7, v11
	v_cvt_pk_bf16_f32 v8, v8, v10
	v_cvt_pk_bf16_f32 v9, v0, v9
	v_add_u32_e32 v0, s81, v171
	s_cmp_eq_u32 s84, 0x2000000
	ds_write_b128 v0, v[2:5]
	ds_write_b128 v0, v[6:9] offset:16
	s_cselect_b32 s77, s77, s57
	s_cselect_b32 s76, s76, s56
	v_mov_b32_e32 v2, v169
	s_lshl_b64 s[54:55], s[76:77], 12
	s_add_u32 vcc_lo, s58, s54
	v_lshlrev_b32_e32 v3, 4, v2
	v_lshlrev_b32_e32 v0, 7, v2
	v_and_b32_e32 v4, 0x1f0, v3
	s_addc_u32 vcc_hi, s59, s55
	v_and_or_b32 v0, v0, s39, v4
	v_lshl_add_u64 v[14:15], vcc, 0, v[0:1]
	v_lshlrev_b32_e32 v198, 10, v2
	v_and_b32_e32 v199, 0x70, v3
	global_load_dwordx4 v[2:5], v0, vcc
	v_add_co_u32_e32 v6, vcc, s33, v14
	s_lshl_b64 s[54:55], s[76:77], 13
	s_nop 0
	v_addc_co_u32_e32 v7, vcc, 0, v15, vcc
	v_add_co_u32_e32 v10, vcc, s40, v14
	s_add_u32 s54, s36, s54
	s_nop 0
	v_addc_co_u32_e32 v11, vcc, 0, v15, vcc
	v_add_co_u32_e32 v80, vcc, s41, v14
	s_addc_u32 s55, s37, s55
	s_nop 0
	v_addc_co_u32_e32 v81, vcc, 0, v15, vcc
	v_add_co_u32_e32 v84, vcc, s42, v14
	v_and_or_b32 v0, v198, s48, v199
	s_nop 0
	v_addc_co_u32_e32 v85, vcc, 0, v15, vcc
	v_add_co_u32_e32 v88, vcc, s43, v14
	v_or_b32_e32 v197, s79, v160
	s_nop 0
	v_addc_co_u32_e32 v89, vcc, 0, v15, vcc
	v_add_co_u32_e32 v92, vcc, s44, v14
	global_load_dwordx4 v[10:13], v[10:11], off
	s_nop 0
	v_addc_co_u32_e32 v93, vcc, 0, v15, vcc
	v_add_co_u32_e32 v14, vcc, s45, v14
	global_load_dwordx4 v[6:9], v[6:7], off
	s_nop 0
	v_addc_co_u32_e32 v15, vcc, 0, v15, vcc
	global_load_dwordx4 v[160:163], v[14:15], off
	v_lshl_add_u64 v[14:15], s[54:55], 0, v[0:1]
	v_add_co_u32_e32 v14, vcc, s49, v14
	global_load_dwordx4 v[80:83], v[80:81], off
	s_nop 0
	v_addc_co_u32_e32 v15, vcc, 0, v15, vcc
	global_load_dwordx4 v[84:87], v[84:85], off
	v_cndmask_b32_e64 v55, v71, v55, s[0:1]
	global_load_dwordx4 v[88:91], v[88:89], off
	v_cndmask_b32_e64 v54, v70, v54, s[0:1]
	global_load_dwordx4 v[92:95], v[92:93], off
	v_cndmask_b32_e64 v53, v69, v53, s[0:1]
	v_cndmask_b32_e64 v52, v68, v52, s[0:1]
	v_cndmask_b32_e64 v51, v67, v51, s[0:1]
	v_cndmask_b32_e64 v50, v66, v50, s[0:1]
	v_cndmask_b32_e64 v49, v65, v49, s[0:1]
	v_cndmask_b32_e64 v48, v64, v48, s[0:1]
	global_load_dwordx4 v[64:67], v0, s[54:55] nt
	global_load_dwordx4 v[68:71], v[14:15], off nt
	s_add_u32 s54, s76, s62
	s_addc_u32 s55, s77, 0
	s_lshr_b64 s[54:55], s[54:55], 2
	s_add_u32 s54, s54, s47
	s_addc_u32 s55, s55, 0
	s_lshl_b64 s[54:55], s[54:55], 14
	v_readlane_b32 s52, v250, 46
	v_or_b32_e32 v207, v195, v196
	v_readlane_b32 s53, v250, 47
	s_add_u32 s76, s52, s54
	v_bitop3_b32 v0, v197, v165, v194 bitop3:0x36
	s_addc_u32 s77, s53, s55
	v_lshl_or_b32 v0, v0, 4, v207
	s_add_i32 s54, 0, 0x18000
	v_add_u32_e32 v14, s54, v0
	v_or_b32_e32 v206, v197, v194
	v_cndmask_b32_e64 v63, v79, v63, s[0:1]
	v_cndmask_b32_e64 v62, v78, v62, s[0:1]
	v_cndmask_b32_e64 v61, v77, v61, s[0:1]
	v_cndmask_b32_e64 v60, v76, v60, s[0:1]
	v_cndmask_b32_e64 v59, v75, v59, s[0:1]
	v_cndmask_b32_e64 v58, v74, v58, s[0:1]
	v_cndmask_b32_e64 v57, v73, v57, s[0:1]
	v_cndmask_b32_e64 v56, v72, v56, s[0:1]
	v_xad_u32 v0, v0, 16, s54
	ds_read_b64_tr_b16 v[72:73], v14
	ds_read_b64_tr_b16 v[74:75], v0 offset:1024
	ds_read_b64_tr_b16 v[76:77], v14 offset:4096
	ds_read_b64_tr_b16 v[78:79], v0 offset:5120
	ds_read_b64_tr_b16 v[194:195], v14 offset:8192
	ds_read_b64_tr_b16 v[196:197], v0 offset:9216
	ds_read_b64_tr_b16 v[198:199], v14 offset:12288
	ds_read_b64_tr_b16 v[200:201], v0 offset:13312
	ds_read_b64_tr_b16 v[202:203], v14 offset:16384
	ds_read_b64_tr_b16 v[204:205], v0 offset:17408
	ds_read_b64_tr_b16 v[212:213], v14 offset:20480
	ds_read_b64_tr_b16 v[214:215], v0 offset:21504
	ds_read_b64_tr_b16 v[216:217], v14 offset:24576
	ds_read_b64_tr_b16 v[218:219], v0 offset:25600
	ds_read_b64_tr_b16 v[220:221], v14 offset:28672
	ds_read_b64_tr_b16 v[222:223], v0 offset:29696
	s_waitcnt lgkmcnt(0)
	s_waitcnt vmcnt(25) lgkmcnt(14)
	v_mfma_f32_32x32x16_bf16 v[48:63], v[72:75], v[144:147], v[48:63]
	v_mov_b32_e32 v0, v168
	s_nop 0
	v_lshlrev_b32_e32 v0, 4, v0
	v_lshl_add_u64 v[14:15], s[76:77], 0, v[0:1]
	v_add_co_u32_e32 v14, vcc, s63, v14
	s_waitcnt vmcnt(24) lgkmcnt(12)
	v_mfma_f32_32x32x16_bf16 v[48:63], v[76:79], v[152:155], v[48:63]
	v_addc_co_u32_e32 v15, vcc, 0, v15, vcc
	global_load_dwordx4 v[144:147], v0, s[76:77]
	global_load_dwordx4 v[152:155], v0, s[76:77] offset:1024
	s_waitcnt vmcnt(25) lgkmcnt(10)
	v_mfma_f32_32x32x16_bf16 v[48:63], v[194:197], v[140:143], v[48:63]
	s_waitcnt vmcnt(24) lgkmcnt(8)
	v_mfma_f32_32x32x16_bf16 v[48:63], v[198:201], v[136:139], v[48:63]
	global_load_dwordx4 v[140:143], v0, s[76:77] offset:2048
	global_load_dwordx4 v[136:139], v0, s[76:77] offset:3072
	s_waitcnt vmcnt(25) lgkmcnt(6)
	v_mfma_f32_32x32x16_bf16 v[48:63], v[202:205], v[156:159], v[48:63]
	s_waitcnt vmcnt(24) lgkmcnt(4)
	v_mfma_f32_32x32x16_bf16 v[48:63], v[212:215], v[148:151], v[48:63]
	global_load_dwordx4 v[156:159], v[14:15], off
	global_load_dwordx4 v[148:151], v[14:15], off offset:1024
	s_waitcnt vmcnt(25) lgkmcnt(2)
	v_mfma_f32_32x32x16_bf16 v[48:63], v[216:219], v[132:135], v[48:63]
	global_load_dwordx4 v[132:135], v[14:15], off offset:2048
	global_load_dwordx4 v[72:75], v[14:15], off offset:3072
	s_waitcnt vmcnt(26) lgkmcnt(0)
	v_mfma_f32_32x32x16_bf16 v[48:63], v[220:223], v[128:131], v[48:63]
	v_bitop3_b32 v0, v206, v165, 8 bitop3:0x36
	v_lshl_add_u32 v0, v0, 4, v207
	v_add_u32_e32 v14, s54, v0
	v_xad_u32 v0, v0, 16, s54
	ds_read_b64_tr_b16 v[76:77], v14
	ds_read_b64_tr_b16 v[128:129], v14 offset:4096
	ds_read_b64_tr_b16 v[194:195], v14 offset:8192
	ds_read_b64_tr_b16 v[198:199], v14 offset:12288
	ds_read_b64_tr_b16 v[78:79], v0 offset:1024
	ds_read_b64_tr_b16 v[130:131], v0 offset:5120
	ds_read_b64_tr_b16 v[196:197], v0 offset:9216
	ds_read_b64_tr_b16 v[200:201], v0 offset:13312
	ds_read_b64_tr_b16 v[202:203], v14 offset:16384
	ds_read_b64_tr_b16 v[212:213], v14 offset:20480
	ds_read_b64_tr_b16 v[216:217], v14 offset:24576
	ds_read_b64_tr_b16 v[220:221], v14 offset:28672
	ds_read_b64_tr_b16 v[204:205], v0 offset:17408
	ds_read_b64_tr_b16 v[214:215], v0 offset:21504
	ds_read_b64_tr_b16 v[218:219], v0 offset:25600
	ds_read_b64_tr_b16 v[222:223], v0 offset:29696
	s_waitcnt lgkmcnt(0)
	s_waitcnt vmcnt(25) lgkmcnt(11)
	v_mfma_f32_32x32x16_bf16 v[48:63], v[76:79], v[124:127], v[48:63]
	v_mov_b32_e32 v0, v168
	s_nop 0
	v_lshlrev_b32_e32 v0, 4, v0
	v_lshl_add_u64 v[14:15], s[76:77], 0, v[0:1]
	v_add_co_u32_e32 v76, vcc, s80, v14
	s_waitcnt vmcnt(24) lgkmcnt(10)
	v_mfma_f32_32x32x16_bf16 v[48:63], v[128:131], v[120:123], v[48:63]
	v_addc_co_u32_e32 v77, vcc, 0, v15, vcc
	v_add_co_u32_e32 v14, vcc, s78, v14
	s_nop 1
	v_addc_co_u32_e32 v15, vcc, 0, v15, vcc
	s_waitcnt vmcnt(23) lgkmcnt(9)
	v_mfma_f32_32x32x16_bf16 v[48:63], v[194:197], v[112:115], v[48:63]
	s_waitcnt vmcnt(22) lgkmcnt(8)
	v_mfma_f32_32x32x16_bf16 v[48:63], v[198:201], v[108:111], v[48:63]
	s_waitcnt vmcnt(21) lgkmcnt(3)
	v_mfma_f32_32x32x16_bf16 v[48:63], v[202:205], v[116:119], v[48:63]
	s_waitcnt vmcnt(20) lgkmcnt(2)
	v_mfma_f32_32x32x16_bf16 v[48:63], v[212:215], v[104:107], v[48:63]
	global_load_dwordx4 v[120:123], v[76:77], off offset:1024
	global_load_dwordx4 v[112:115], v[76:77], off offset:2048
	global_load_dwordx4 v[124:127], v[14:15], off offset:-4096
	global_load_dwordx4 v[108:111], v[76:77], off offset:3072
	global_load_dwordx4 v[116:119], v[14:15], off
	global_load_dwordx4 v[104:107], v[14:15], off offset:1024
	s_waitcnt vmcnt(25) lgkmcnt(1)
	v_mfma_f32_32x32x16_bf16 v[48:63], v[216:219], v[100:103], v[48:63]
	global_load_dwordx4 v[100:103], v[14:15], off offset:2048
	global_load_dwordx4 v[76:79], v[14:15], off offset:3072
	s_waitcnt vmcnt(26) lgkmcnt(0)
	v_mfma_f32_32x32x16_bf16 v[48:63], v[220:223], v[96:99], v[48:63]
	v_mov_b32_e32 v0, v168
	v_add_u32_e32 v14, s66, v171
	s_barrier
	ds_read_b128 v[96:99], v14
	ds_read_b128 v[128:131], v14 offset:16
	s_add_u32 s54, s38, s84
	s_addc_u32 s55, s60, s85
	s_waitcnt lgkmcnt(1)
	v_lshlrev_b32_e32 v14, 16, v96
	s_nop 2
	v_add_f32_e32 v14, v48, v14
	s_waitcnt lgkmcnt(0)
	v_lshlrev_b32_e32 v48, 16, v128
	v_add_f32_e32 v56, v56, v48
	v_and_b32_e32 v48, 0xffff0000, v128
	v_and_b32_e32 v15, 0xffff0000, v96
	v_add_f32_e32 v57, v57, v48
	v_lshlrev_b32_e32 v48, 16, v97
	v_add_f32_e32 v15, v49, v15
	v_add_f32_e32 v49, v50, v48
	v_and_b32_e32 v48, 0xffff0000, v97
	v_add_f32_e32 v50, v51, v48
	v_lshlrev_b32_e32 v48, 16, v129
	v_add_f32_e32 v58, v58, v48
	v_and_b32_e32 v48, 0xffff0000, v129
	v_add_f32_e32 v59, v59, v48
	v_lshlrev_b32_e32 v48, 16, v98
	v_add_f32_e32 v51, v52, v48
	v_and_b32_e32 v48, 0xffff0000, v98
	v_add_f32_e32 v52, v53, v48
	v_lshlrev_b32_e32 v48, 16, v130
	v_add_f32_e32 v60, v60, v48
	v_and_b32_e32 v48, 0xffff0000, v130
	v_add_f32_e32 v61, v61, v48
	v_lshlrev_b32_e32 v48, 16, v99
	v_add_f32_e32 v53, v54, v48
	v_and_b32_e32 v48, 0xffff0000, v99
	v_add_f32_e32 v54, v55, v48
	v_lshlrev_b32_e32 v48, 16, v131
	v_add_f32_e32 v55, v62, v48
	v_and_b32_e32 v48, 0xffff0000, v131
	v_add_f32_e32 v62, v63, v48
	v_lshlrev_b32_e32 v48, 13, v0
	v_lshrrev_b32_e32 v0, 1, v0
	v_and_b32_e32 v48, 0x3e000, v48
	v_and_b32_e32 v0, 0x7ffffff0, v0
	v_mul_f32_e32 v14, v193, v14
	v_mul_f32_e32 v15, v193, v15
	v_add_u32_e32 v0, v48, v0
	v_cvt_pk_bf16_f32 v48, v14, v15
	v_mul_f32_e32 v14, v193, v49
	v_mul_f32_e32 v15, v193, v50
	v_cvt_pk_bf16_f32 v49, v14, v15
	v_mul_f32_e32 v14, v193, v51
	v_mul_f32_e32 v15, v193, v52
	v_cvt_pk_bf16_f32 v50, v14, v15
	v_mul_f32_e32 v14, v193, v53
	v_mul_f32_e32 v15, v193, v54
	v_cvt_pk_bf16_f32 v51, v14, v15
	v_mul_f32_e32 v14, v193, v56
	v_mul_f32_e32 v15, v193, v57
	v_cvt_pk_bf16_f32 v52, v14, v15
	v_mul_f32_e32 v14, v193, v58
	v_mul_f32_e32 v15, v193, v59
	v_cvt_pk_bf16_f32 v53, v14, v15
	v_mul_f32_e32 v14, v193, v60
	v_mul_f32_e32 v15, v193, v61
	v_cvt_pk_bf16_f32 v54, v14, v15
	v_mul_f32_e32 v14, v193, v55
	v_mul_f32_e32 v15, v193, v62
	v_cvt_pk_bf16_f32 v55, v14, v15
	v_lshl_add_u64 v[14:15], s[54:55], 0, v[0:1]
	s_mov_b32 s54, 0x2bc00000
	v_add_co_u32_e32 v14, vcc, s54, v14
	v_permlane32_swap_b32_e32 v48, v50
	v_permlane32_swap_b32_e32 v49, v51
	v_addc_co_u32_e32 v15, vcc, 0, v15, vcc
	v_permlane32_swap_b32_e32 v52, v54
	v_permlane32_swap_b32_e32 v53, v55
	v_mov_b32_e32 v0, v168
	global_store_dwordx4 v[14:15], v[48:51], off
	global_store_dwordx4 v[14:15], v[52:55], off offset:32
	s_nop 0
	v_lshrrev_b32_e32 v14, 3, v0
	v_and_b32_e32 v14, 2, v14
	v_bfe_u32 v15, v0, 1, 1
	v_and_b32_e32 v49, 12, v0
	v_lshrrev_b32_e32 v50, 4, v0
	v_and_or_b32 v49, v50, 2, v49
	v_or_b32_e32 v50, v14, v15
	v_lshlrev_b32_e32 v48, 6, v0
	v_bitop3_b32 v51, v50, v49, s65 bitop3:0x36
	v_lshlrev_b32_e32 v0, 3, v0
	v_and_b32_e32 v48, 0xfffffb00, v48
	v_lshlrev_b32_e32 v51, 4, v51
	v_and_b32_e32 v0, 8, v0
	v_bitop3_b32 v14, v14, v49, v15 bitop3:0x36
	v_bitop3_b32 v15, v50, v49, 4 bitop3:0x36
	v_or3_b32 v51, v51, v48, v0
	v_lshlrev_b32_e32 v14, 4, v14
	v_lshlrev_b32_e32 v15, 4, v15
	v_or3_b32 v14, v14, v48, v0
	v_or3_b32 v0, v15, v48, v0
	v_add_u32_e32 v15, s64, v51
	v_xad_u32 v165, v51, 16, s64
	v_add_u32_e32 v194, s67, v14
	v_xad_u32 v14, v14, 16, s67
	v_add_u32_e32 v195, s67, v0
	v_xad_u32 v0, v0, 16, s67
	ds_read_b64_tr_b16 v[48:49], v15
	ds_read_b64_tr_b16 v[50:51], v165 offset:1024
	ds_read_b64_tr_b16 v[54:55], v165 offset:5120
	ds_read_b64_tr_b16 v[52:53], v15 offset:4096
	ds_read_b64_tr_b16 v[56:57], v194
	ds_read_b64_tr_b16 v[58:59], v14 offset:1024
	ds_read_b64_tr_b16 v[62:63], v14 offset:5120
	ds_read_b64_tr_b16 v[60:61], v194 offset:4096
	ds_read_b64_tr_b16 v[96:97], v195
	ds_read_b64_tr_b16 v[98:99], v0 offset:1024
	ds_read_b64_tr_b16 v[130:131], v0 offset:5120
	ds_read_b64_tr_b16 v[128:129], v195 offset:4096
	s_waitcnt lgkmcnt(0)
	s_waitcnt lgkmcnt(6)
	v_mfma_f32_32x32x16_bf16 v[16:31], v[56:59], v[48:51], v[16:31]
	s_waitcnt lgkmcnt(2)
	v_mfma_f32_32x32x16_bf16 v[32:47], v[96:99], v[48:51], v[32:47]
	v_mfma_f32_32x32x16_bf16 v[16:31], v[60:63], v[52:55], v[16:31]
	s_waitcnt lgkmcnt(0)
	v_mfma_f32_32x32x16_bf16 v[32:47], v[128:131], v[52:55], v[32:47]
	ds_read_b64_tr_b16 v[48:49], v15 offset:8192
	ds_read_b64_tr_b16 v[50:51], v165 offset:9216
	ds_read_b64_tr_b16 v[54:55], v165 offset:13312
	ds_read_b64_tr_b16 v[52:53], v15 offset:12288
	ds_read_b64_tr_b16 v[56:57], v194 offset:8192
	ds_read_b64_tr_b16 v[58:59], v14 offset:9216
	ds_read_b64_tr_b16 v[62:63], v14 offset:13312
	ds_read_b64_tr_b16 v[60:61], v194 offset:12288
	ds_read_b64_tr_b16 v[96:97], v195 offset:8192
	ds_read_b64_tr_b16 v[98:99], v0 offset:9216
	ds_read_b64_tr_b16 v[130:131], v0 offset:13312
	ds_read_b64_tr_b16 v[128:129], v195 offset:12288
	s_waitcnt lgkmcnt(0)
	s_waitcnt lgkmcnt(6)
	v_mfma_f32_32x32x16_bf16 v[16:31], v[56:59], v[48:51], v[16:31]
	s_waitcnt lgkmcnt(2)
	v_mfma_f32_32x32x16_bf16 v[32:47], v[96:99], v[48:51], v[32:47]
	v_mfma_f32_32x32x16_bf16 v[16:31], v[60:63], v[52:55], v[16:31]
	s_waitcnt lgkmcnt(0)
	v_mfma_f32_32x32x16_bf16 v[32:47], v[128:131], v[52:55], v[32:47]
	ds_read_b64_tr_b16 v[48:49], v15 offset:16384
	ds_read_b64_tr_b16 v[50:51], v165 offset:17408
	ds_read_b64_tr_b16 v[54:55], v165 offset:21504
	ds_read_b64_tr_b16 v[52:53], v15 offset:20480
	ds_read_b64_tr_b16 v[56:57], v194 offset:16384
	ds_read_b64_tr_b16 v[58:59], v14 offset:17408
	ds_read_b64_tr_b16 v[62:63], v14 offset:21504
	ds_read_b64_tr_b16 v[60:61], v194 offset:20480
	ds_read_b64_tr_b16 v[96:97], v195 offset:16384
	ds_read_b64_tr_b16 v[98:99], v0 offset:17408
	ds_read_b64_tr_b16 v[130:131], v0 offset:21504
	ds_read_b64_tr_b16 v[128:129], v195 offset:20480
	s_waitcnt lgkmcnt(0)
	s_waitcnt lgkmcnt(6)
	v_mfma_f32_32x32x16_bf16 v[16:31], v[56:59], v[48:51], v[16:31]
	s_waitcnt lgkmcnt(2)
	v_mfma_f32_32x32x16_bf16 v[32:47], v[96:99], v[48:51], v[32:47]
	v_mfma_f32_32x32x16_bf16 v[16:31], v[60:63], v[52:55], v[16:31]
	s_waitcnt lgkmcnt(0)
	v_mfma_f32_32x32x16_bf16 v[32:47], v[128:131], v[52:55], v[32:47]
	ds_read_b64_tr_b16 v[48:49], v15 offset:24576
	ds_read_b64_tr_b16 v[50:51], v165 offset:25600
	ds_read_b64_tr_b16 v[54:55], v165 offset:29696
	ds_read_b64_tr_b16 v[52:53], v15 offset:28672
	ds_read_b64_tr_b16 v[56:57], v194 offset:24576
	ds_read_b64_tr_b16 v[58:59], v14 offset:25600
	ds_read_b64_tr_b16 v[62:63], v14 offset:29696
	ds_read_b64_tr_b16 v[60:61], v194 offset:28672
	ds_read_b64_tr_b16 v[96:97], v195 offset:24576
	ds_read_b64_tr_b16 v[98:99], v0 offset:25600
	ds_read_b64_tr_b16 v[130:131], v0 offset:29696
	ds_read_b64_tr_b16 v[128:129], v195 offset:28672
	s_waitcnt lgkmcnt(0)
	s_waitcnt lgkmcnt(6)
	v_mfma_f32_32x32x16_bf16 v[16:31], v[56:59], v[48:51], v[16:31]
	s_waitcnt lgkmcnt(2)
	v_mfma_f32_32x32x16_bf16 v[32:47], v[96:99], v[48:51], v[32:47]
	v_mfma_f32_32x32x16_bf16 v[16:31], v[60:63], v[52:55], v[16:31]
	s_waitcnt lgkmcnt(0)
	v_mfma_f32_32x32x16_bf16 v[32:47], v[128:131], v[52:55], v[32:47]
	v_mov_b32_e32 v165, v164
	s_nop 8
	v_mul_f32_e64 v18, v164, v18
	v_mul_f32_e64 v19, v165, v19
	v_mul_f32_e64 v16, v166, v16
	v_mul_f32_e64 v17, v167, v17
	v_pk_mul_f32 v[22:23], v[164:165], v[22:23]
	v_cvt_pk_bf16_f32 v14, v16, v17
	v_cvt_pk_bf16_f32 v15, v18, v19
	v_pk_mul_f32 v[20:21], v[164:165], v[20:21]
	v_pk_mul_f32 v[34:35], v[164:165], v[34:35]
	v_pk_mul_f32 v[32:33], v[166:167], v[32:33]
	s_add_u32 s84, s84, 0x100000
	v_cvt_pk_bf16_f32 v48, v32, v33
	v_cvt_pk_bf16_f32 v49, v34, v35
	ds_write_b64 v185, v[14:15]
	ds_write_b64 v186, v[48:49]
	v_cvt_pk_bf16_f32 v14, v20, v21
	v_cvt_pk_bf16_f32 v15, v22, v23
	v_pk_mul_f32 v[26:27], v[164:165], v[26:27]
	v_pk_mul_f32 v[24:25], v[164:165], v[24:25]
	v_pk_mul_f32 v[38:39], v[164:165], v[38:39]
	v_pk_mul_f32 v[36:37], v[164:165], v[36:37]
	s_addc_u32 s85, s85, 0
	v_cvt_pk_bf16_f32 v48, v36, v37
	v_cvt_pk_bf16_f32 v49, v38, v39
	ds_write_b64 v187, v[14:15]
	ds_write_b64 v188, v[48:49]
	v_cvt_pk_bf16_f32 v14, v24, v25
	v_cvt_pk_bf16_f32 v15, v26, v27
	s_waitcnt vmcnt(2)
	v_mov_b64_e32 v[98:99], v[78:79]
	v_mov_b64_e32 v[130:131], v[74:75]
	v_pk_mul_f32 v[30:31], v[164:165], v[30:31]
	v_pk_mul_f32 v[28:29], v[164:165], v[28:29]
	v_pk_mul_f32 v[46:47], v[164:165], v[46:47]
	v_pk_mul_f32 v[44:45], v[164:165], v[44:45]
	v_pk_mul_f32 v[42:43], v[164:165], v[42:43]
	v_pk_mul_f32 v[40:41], v[164:165], v[40:41]
	s_cmp_eq_u32 s84, 0x2100000
	v_cvt_pk_bf16_f32 v48, v40, v41
	v_cvt_pk_bf16_f32 v49, v42, v43
	ds_write_b64 v189, v[14:15]
	ds_write_b64 v190, v[48:49]
	v_cvt_pk_bf16_f32 v14, v28, v29
	v_cvt_pk_bf16_f32 v15, v30, v31
	s_mov_b64 s[76:77], s[56:57]
	v_mov_b64_e32 v[96:97], v[76:77]
	v_mov_b64_e32 v[128:129], v[72:73]
	v_cvt_pk_bf16_f32 v48, v44, v45
	v_cvt_pk_bf16_f32 v49, v46, v47
	ds_write_b64 v191, v[14:15]
	ds_write_b64 v192, v[48:49]
	s_cbranch_scc1 .LBB0_261

.LBB0_1086:
	v_mbcnt_lo_u32_b32 v146, -1, 0
	v_mbcnt_hi_u32_b32 v146, -1, v146
	s_and_b64 s[2:3], s[4:5], exec
	v_ashrrev_i32_e32 v4, 5, v146
	v_ashrrev_i32_e32 v11, 4, v146
	v_and_b32_e32 v13, 15, v146
	v_lshrrev_b32_e32 v0, 1, v146
	v_mov_b32_e32 v7, s56
	v_lshlrev_b32_e32 v7, 1, v7
	v_and_b32_e32 v7, 8, v7
	v_or_b32_e32 v7, v7, v11
	v_xor_b32_e32 v7, v7, v13
	v_add_u32_e32 v8, s56, v4
	v_bfe_u32 v2, v146, 2, 2
	v_and_b32_e32 v5, 8, v0
	v_lshlrev_b32_e32 v10, 4, v7
	v_lshlrev_b32_e32 v7, 1, v8
	v_or_b32_e32 v14, v5, v2
	v_and_b32_e32 v7, -16, v7
	v_and_b32_e32 v8, 4, v8
	v_lshlrev_b32_e32 v12, 4, v146
	v_or3_b32 v15, v8, v7, v14
	v_lshlrev_b32_e32 v9, 6, v4
	v_and_b32_e32 v3, 48, v12
	v_and_b32_e32 v9, 0xc0, v9
	v_lshlrev_b32_e32 v15, 12, v15
	v_or3_b32 v19, v15, v9, v3
	v_add_u32_e32 v15, s57, v11
	v_lshlrev_b32_e32 v6, 12, v11
	v_bitop3_b32 v11, v15, v13, 15 bitop3:0x6c
	v_lshlrev_b32_e32 v11, 4, v11
	s_cselect_b32 s6, s76, s77
	v_lshl_or_b32 v13, v15, 12, v11
	v_add_u32_e32 v15, s58, v4
	s_or_b32 s44, s6, 0x80
	v_lshlrev_b32_e32 v16, 1, v15
	s_add_u32 s2, s71, s44
	v_and_b32_e32 v16, 0xffff0, v16
	v_and_b32_e32 v17, 4, v15
	s_addc_u32 s3, s70, 0
	v_or3_b32 v14, v17, v16, v14
	v_lshlrev_b32_e32 v15, 6, v15
	s_lshl_b64 s[36:37], s[2:3], 12
	v_and_b32_e32 v145, 31, v146
	v_and_b32_e32 v15, 0xc0, v15
	v_lshlrev_b32_e32 v14, 12, v14
	s_add_u32 s2, s79, s36
	v_or3_b32 v20, v14, v15, v3
	v_or_b32_e32 v14, s8, v145
	s_addc_u32 s3, s81, s37
	v_ashrrev_i32_e32 v15, 31, v14
	s_add_i32 s7, s6, 0x17f
	v_lshlrev_b64 v[14:15], 12, v[14:15]
	v_lshlrev_b32_e32 v16, 3, v4
	s_and_b32 s38, s7, 0x1f40
	v_lshl_add_u64 v[14:15], s[2:3], 0, v[14:15]
	v_ashrrev_i32_e32 v17, 31, v16
	s_lshl_b32 s33, s38, 12
	v_lshl_add_u64 v[14:15], v[16:17], 1, v[14:15]
	s_add_u32 s2, s82, s33
	global_load_dwordx4 v[112:115], v[14:15], off nt
	global_load_dwordx4 v[116:119], v[14:15], off offset:32 nt
	global_load_dwordx4 v[120:123], v[14:15], off offset:64 nt
	global_load_dwordx4 v[124:127], v[14:15], off offset:96 nt
	global_load_dwordx4 v[128:131], v[14:15], off offset:128 nt
	global_load_dwordx4 v[132:135], v[14:15], off offset:160 nt
	global_load_dwordx4 v[136:139], v[14:15], off offset:192 nt
	global_load_dwordx4 v[140:143], v[14:15], off offset:224 nt
	s_addc_u32 s3, s83, 0
	s_add_u32 s34, s84, s33
	v_add_u32_e32 v0, s55, v6
	s_addc_u32 s35, s85, 0
	s_add_i32 s33, s68, 0x8000
	v_or_b32_e32 v18, v10, v0
	s_mov_b32 m0, s33
	v_add_u32_e32 v14, s38, v146
	global_load_lds_dwordx4 v18, s[2:3]
	s_mov_b32 m0, s68
	s_add_i32 s42, s68, 0x8400
	v_ashrrev_i32_e32 v15, 31, v14
	global_load_lds_dwordx4 v19, s[34:35]
	s_mov_b32 m0, s42
	s_add_i32 s43, s68, 0x400
	v_lshl_add_u64 v[14:15], v[14:15], 2, s[30:31]
	global_load_lds_dwordx4 v13, s[2:3]
	s_mov_b32 m0, s43
	global_load_dword v172, v[14:15], off
	v_cmp_ne_u32_e64 s[2:3], 1, v158
	global_load_lds_dwordx4 v20, s[34:35]
	s_andn2_b64 vcc, exec, s[10:11]
	s_cbranch_vccnz .LBB0_1088
	v_lshl_add_u32 v13, v146, 2, 0
	v_add_u32_e32 v13, 0x10800, v13
	s_waitcnt vmcnt(0)
	ds_write_b32 v13, v172
